# GEMM loop: snake j-order on alternate rows so consecutive MFMAs across a row boundary share the B fragment
# baseline (speedup 1.0000x reference)
.Lgemm_T_loop:
	s_waitcnt lgkmcnt(9)
	s_add_u32 m0, s11, 0x1e080
	v_mfma_f32_16x16x32_f16 v[82:85], v[134:137], v[86:89], v[82:85]
	global_load_lds_dwordx4 v[220:221], off offset:-128
	v_mfma_f32_16x16x32_f16 v[58:61], v[138:141], v[86:89], v[58:61]
	v_mfma_f32_16x16x32_f16 v[14:17], v[142:145], v[86:89], v[14:17]
	v_mfma_f32_16x16x32_f16 v[30:33], v[142:145], v[90:93], v[30:33]
	v_mfma_f32_16x16x32_f16 v[22:25], v[138:141], v[90:93], v[22:25]
	v_mfma_f32_16x16x32_f16 v[78:81], v[134:137], v[90:93], v[78:81]
	s_add_u32 m0, s11, 0x20080
	v_mfma_f32_16x16x32_f16 v[74:77], v[134:137], v[94:97], v[74:77]
	global_load_lds_dwordx4 v[224:225], off offset:-128
	v_mfma_f32_16x16x32_f16 v[18:21], v[138:141], v[94:97], v[18:21]
	v_mfma_f32_16x16x32_f16 v[26:29], v[142:145], v[94:97], v[26:29]
	v_mfma_f32_16x16x32_f16 v[240:243], v[142:145], v[98:101], v[240:243]
	v_mfma_f32_16x16x32_f16 v[46:49], v[138:141], v[98:101], v[46:49]
	v_mfma_f32_16x16x32_f16 v[70:73], v[134:137], v[98:101], v[70:73]
	s_add_u32 m0, s11, 0x22080
	v_mfma_f32_16x16x32_f16 v[66:69], v[134:137], v[102:105], v[66:69]
	global_load_lds_dwordx4 v[228:229], off offset:-128
	v_mfma_f32_16x16x32_f16 v[42:45], v[138:141], v[102:105], v[42:45]
	v_mfma_f32_16x16x32_f16 v[236:239], v[142:145], v[102:105], v[236:239]
	v_mfma_f32_16x16x32_f16 v[34:37], v[142:145], v[106:109], v[34:37]
	v_mfma_f32_16x16x32_f16 v[38:41], v[138:141], v[106:109], v[38:41]
	v_mfma_f32_16x16x32_f16 v[62:65], v[134:137], v[106:109], v[62:65]
	s_waitcnt vmcnt(6) lgkmcnt(0)
	s_barrier
	s_add_u32 m0, s11, 0x0
	ds_read_b128 v[134:137], v162 offset:49152
	global_load_lds_dwordx4 v[218:219], off
	v_mfma_f32_16x16x32_f16 v[82:85], v[146:149], v[110:113], v[82:85]
	ds_read_b128 v[138:141], v162 offset:51200
	v_mfma_f32_16x16x32_f16 v[58:61], v[150:153], v[110:113], v[58:61]
	ds_read_b128 v[142:145], v162 offset:53248
	v_mfma_f32_16x16x32_f16 v[14:17], v[154:157], v[110:113], v[14:17]
	ds_read_b128 v[86:89], v158 offset:49152
	v_mfma_f32_16x16x32_f16 v[30:33], v[154:157], v[114:117], v[30:33]
	ds_read_b128 v[90:93], v158 offset:51200
	v_mfma_f32_16x16x32_f16 v[22:25], v[150:153], v[114:117], v[22:25]
	ds_read_b128 v[94:97], v158 offset:53248
	v_mfma_f32_16x16x32_f16 v[78:81], v[146:149], v[114:117], v[78:81]
	s_add_u32 m0, s11, 0x2000
	ds_read_b128 v[98:101], v158 offset:55296
	global_load_lds_dwordx4 v[222:223], off
	v_mfma_f32_16x16x32_f16 v[74:77], v[146:149], v[118:121], v[74:77]
	ds_read_b128 v[102:105], v158 offset:57344
	v_mfma_f32_16x16x32_f16 v[18:21], v[150:153], v[118:121], v[18:21]
	ds_read_b128 v[106:109], v158 offset:59392
	v_mfma_f32_16x16x32_f16 v[26:29], v[154:157], v[118:121], v[26:29]
	ds_read_b128 v[110:113], v160 offset:49152
	v_mfma_f32_16x16x32_f16 v[240:243], v[154:157], v[122:125], v[240:243]
	ds_read_b128 v[114:117], v160 offset:51200
	v_mfma_f32_16x16x32_f16 v[46:49], v[150:153], v[122:125], v[46:49]
	v_mfma_f32_16x16x32_f16 v[70:73], v[146:149], v[122:125], v[70:73]
	s_add_u32 m0, s11, 0x4000
	ds_read_b128 v[118:121], v160 offset:53248
	global_load_lds_dwordx4 v[226:227], off
	v_mfma_f32_16x16x32_f16 v[66:69], v[146:149], v[126:129], v[66:69]
	ds_read_b128 v[122:125], v160 offset:55296
	v_mfma_f32_16x16x32_f16 v[42:45], v[150:153], v[126:129], v[42:45]
	v_mfma_f32_16x16x32_f16 v[236:239], v[154:157], v[126:129], v[236:239]
	ds_read_b128 v[126:129], v160 offset:57344
	v_mfma_f32_16x16x32_f16 v[34:37], v[154:157], v[130:133], v[34:37]
	v_mfma_f32_16x16x32_f16 v[38:41], v[150:153], v[130:133], v[38:41]
	v_mfma_f32_16x16x32_f16 v[62:65], v[146:149], v[130:133], v[62:65]
	ds_read_b128 v[130:133], v160 offset:59392
	ds_read_b128 v[146:149], v164 offset:49152
	ds_read_b128 v[150:153], v164 offset:51200
	ds_read_b128 v[154:157], v164 offset:53248
	s_waitcnt lgkmcnt(9)
	s_add_u32 m0, s11, 0x6000
	v_mfma_f32_16x16x32_f16 v[82:85], v[134:137], v[86:89], v[82:85]
	global_load_lds_dwordx4 v[220:221], off
	v_mfma_f32_16x16x32_f16 v[58:61], v[138:141], v[86:89], v[58:61]
	v_mfma_f32_16x16x32_f16 v[14:17], v[142:145], v[86:89], v[14:17]
	v_mfma_f32_16x16x32_f16 v[30:33], v[142:145], v[90:93], v[30:33]
	v_mfma_f32_16x16x32_f16 v[22:25], v[138:141], v[90:93], v[22:25]
	v_mfma_f32_16x16x32_f16 v[78:81], v[134:137], v[90:93], v[78:81]
	s_add_u32 m0, s11, 0x8000
	v_mfma_f32_16x16x32_f16 v[74:77], v[134:137], v[94:97], v[74:77]
	global_load_lds_dwordx4 v[224:225], off
	v_mfma_f32_16x16x32_f16 v[18:21], v[138:141], v[94:97], v[18:21]
	v_mfma_f32_16x16x32_f16 v[26:29], v[142:145], v[94:97], v[26:29]
	v_mfma_f32_16x16x32_f16 v[240:243], v[142:145], v[98:101], v[240:243]
	v_mfma_f32_16x16x32_f16 v[46:49], v[138:141], v[98:101], v[46:49]
	v_mfma_f32_16x16x32_f16 v[70:73], v[134:137], v[98:101], v[70:73]
	s_add_u32 m0, s11, 0xa000
	v_mfma_f32_16x16x32_f16 v[66:69], v[134:137], v[102:105], v[66:69]
	global_load_lds_dwordx4 v[228:229], off
	v_mfma_f32_16x16x32_f16 v[42:45], v[138:141], v[102:105], v[42:45]
	v_mfma_f32_16x16x32_f16 v[236:239], v[142:145], v[102:105], v[236:239]
	v_mfma_f32_16x16x32_f16 v[34:37], v[142:145], v[106:109], v[34:37]
	v_mfma_f32_16x16x32_f16 v[38:41], v[138:141], v[106:109], v[38:41]
	v_mfma_f32_16x16x32_f16 v[62:65], v[134:137], v[106:109], v[62:65]
	s_waitcnt vmcnt(6) lgkmcnt(0)
	s_barrier
	s_add_u32 m0, s11, 0xbf80
	ds_read_b128 v[134:137], v163
	global_load_lds_dwordx4 v[218:219], off offset:128
	v_mfma_f32_16x16x32_f16 v[82:85], v[146:149], v[110:113], v[82:85]
	ds_read_b128 v[138:141], v163 offset:2048
	v_mfma_f32_16x16x32_f16 v[58:61], v[150:153], v[110:113], v[58:61]
	ds_read_b128 v[142:145], v163 offset:4096
	v_mfma_f32_16x16x32_f16 v[14:17], v[154:157], v[110:113], v[14:17]
	ds_read_b128 v[86:89], v159
	v_mfma_f32_16x16x32_f16 v[30:33], v[154:157], v[114:117], v[30:33]
	ds_read_b128 v[90:93], v159 offset:2048
	v_mfma_f32_16x16x32_f16 v[22:25], v[150:153], v[114:117], v[22:25]
	ds_read_b128 v[94:97], v159 offset:4096
	v_mfma_f32_16x16x32_f16 v[78:81], v[146:149], v[114:117], v[78:81]
	s_add_u32 m0, s11, 0xdf80
	ds_read_b128 v[98:101], v159 offset:6144
	global_load_lds_dwordx4 v[222:223], off offset:128
	v_mfma_f32_16x16x32_f16 v[74:77], v[146:149], v[118:121], v[74:77]
	ds_read_b128 v[102:105], v159 offset:8192
	v_mfma_f32_16x16x32_f16 v[18:21], v[150:153], v[118:121], v[18:21]
	ds_read_b128 v[106:109], v159 offset:10240
	v_mfma_f32_16x16x32_f16 v[26:29], v[154:157], v[118:121], v[26:29]
	ds_read_b128 v[110:113], v161
	v_mfma_f32_16x16x32_f16 v[240:243], v[154:157], v[122:125], v[240:243]
	ds_read_b128 v[114:117], v161 offset:2048
	v_mfma_f32_16x16x32_f16 v[46:49], v[150:153], v[122:125], v[46:49]
	v_mfma_f32_16x16x32_f16 v[70:73], v[146:149], v[122:125], v[70:73]
	s_add_u32 m0, s11, 0xff80
	ds_read_b128 v[118:121], v161 offset:4096
	global_load_lds_dwordx4 v[226:227], off offset:128
	v_mfma_f32_16x16x32_f16 v[66:69], v[146:149], v[126:129], v[66:69]
	ds_read_b128 v[122:125], v161 offset:6144
	v_mfma_f32_16x16x32_f16 v[42:45], v[150:153], v[126:129], v[42:45]
	v_mfma_f32_16x16x32_f16 v[236:239], v[154:157], v[126:129], v[236:239]
	ds_read_b128 v[126:129], v161 offset:8192
	v_mfma_f32_16x16x32_f16 v[34:37], v[154:157], v[130:133], v[34:37]
	v_mfma_f32_16x16x32_f16 v[38:41], v[150:153], v[130:133], v[38:41]
	v_mfma_f32_16x16x32_f16 v[62:65], v[146:149], v[130:133], v[62:65]
	ds_read_b128 v[130:133], v161 offset:10240
	ds_read_b128 v[146:149], v165
	ds_read_b128 v[150:153], v165 offset:2048
	ds_read_b128 v[154:157], v165 offset:4096
	s_waitcnt lgkmcnt(9)
	s_add_u32 m0, s11, 0x11f80
	v_mfma_f32_16x16x32_f16 v[82:85], v[134:137], v[86:89], v[82:85]
	global_load_lds_dwordx4 v[220:221], off offset:128
	v_mfma_f32_16x16x32_f16 v[58:61], v[138:141], v[86:89], v[58:61]
	v_mfma_f32_16x16x32_f16 v[14:17], v[142:145], v[86:89], v[14:17]
	v_mfma_f32_16x16x32_f16 v[30:33], v[142:145], v[90:93], v[30:33]
	v_mfma_f32_16x16x32_f16 v[22:25], v[138:141], v[90:93], v[22:25]
	v_mfma_f32_16x16x32_f16 v[78:81], v[134:137], v[90:93], v[78:81]
	s_add_u32 m0, s11, 0x13f80
	v_mfma_f32_16x16x32_f16 v[74:77], v[134:137], v[94:97], v[74:77]
	global_load_lds_dwordx4 v[224:225], off offset:128
	v_mfma_f32_16x16x32_f16 v[18:21], v[138:141], v[94:97], v[18:21]
	v_mfma_f32_16x16x32_f16 v[26:29], v[142:145], v[94:97], v[26:29]
	v_mfma_f32_16x16x32_f16 v[240:243], v[142:145], v[98:101], v[240:243]
	v_mfma_f32_16x16x32_f16 v[46:49], v[138:141], v[98:101], v[46:49]
	v_mfma_f32_16x16x32_f16 v[70:73], v[134:137], v[98:101], v[70:73]
	s_add_u32 m0, s11, 0x15f80
	v_mfma_f32_16x16x32_f16 v[66:69], v[134:137], v[102:105], v[66:69]
	global_load_lds_dwordx4 v[228:229], off offset:128
	v_mfma_f32_16x16x32_f16 v[42:45], v[138:141], v[102:105], v[42:45]
	v_mfma_f32_16x16x32_f16 v[236:239], v[142:145], v[102:105], v[236:239]
	v_mfma_f32_16x16x32_f16 v[34:37], v[142:145], v[106:109], v[34:37]
	v_mfma_f32_16x16x32_f16 v[38:41], v[138:141], v[106:109], v[38:41]
	v_mfma_f32_16x16x32_f16 v[62:65], v[134:137], v[106:109], v[62:65]
	s_waitcnt vmcnt(6) lgkmcnt(0)
	s_barrier
	s_add_u32 m0, s11, 0x17f00
	ds_read_b128 v[134:137], v162
	global_load_lds_dwordx4 v[218:219], off offset:256
	v_mfma_f32_16x16x32_f16 v[82:85], v[146:149], v[110:113], v[82:85]
	ds_read_b128 v[138:141], v162 offset:2048
	v_mfma_f32_16x16x32_f16 v[58:61], v[150:153], v[110:113], v[58:61]
	ds_read_b128 v[142:145], v162 offset:4096
	v_mfma_f32_16x16x32_f16 v[14:17], v[154:157], v[110:113], v[14:17]
	ds_read_b128 v[86:89], v158
	v_mfma_f32_16x16x32_f16 v[30:33], v[154:157], v[114:117], v[30:33]
	ds_read_b128 v[90:93], v158 offset:2048
	v_mfma_f32_16x16x32_f16 v[22:25], v[150:153], v[114:117], v[22:25]
	ds_read_b128 v[94:97], v158 offset:4096
	v_mfma_f32_16x16x32_f16 v[78:81], v[146:149], v[114:117], v[78:81]
	s_add_u32 m0, s11, 0x19f00
	ds_read_b128 v[98:101], v158 offset:6144
	global_load_lds_dwordx4 v[222:223], off offset:256
	v_mfma_f32_16x16x32_f16 v[74:77], v[146:149], v[118:121], v[74:77]
	ds_read_b128 v[102:105], v158 offset:8192
	v_mfma_f32_16x16x32_f16 v[18:21], v[150:153], v[118:121], v[18:21]
	ds_read_b128 v[106:109], v158 offset:10240
	v_mfma_f32_16x16x32_f16 v[26:29], v[154:157], v[118:121], v[26:29]
	ds_read_b128 v[110:113], v160
	v_mfma_f32_16x16x32_f16 v[240:243], v[154:157], v[122:125], v[240:243]
	ds_read_b128 v[114:117], v160 offset:2048
	v_mfma_f32_16x16x32_f16 v[46:49], v[150:153], v[122:125], v[46:49]
	v_mfma_f32_16x16x32_f16 v[70:73], v[146:149], v[122:125], v[70:73]
	s_add_u32 m0, s11, 0x1bf00
	ds_read_b128 v[118:121], v160 offset:4096
	global_load_lds_dwordx4 v[226:227], off offset:256
	v_mfma_f32_16x16x32_f16 v[66:69], v[146:149], v[126:129], v[66:69]
	ds_read_b128 v[122:125], v160 offset:6144
	v_mfma_f32_16x16x32_f16 v[42:45], v[150:153], v[126:129], v[42:45]
	v_mfma_f32_16x16x32_f16 v[236:239], v[154:157], v[126:129], v[236:239]
	ds_read_b128 v[126:129], v160 offset:8192
	v_mfma_f32_16x16x32_f16 v[34:37], v[154:157], v[130:133], v[34:37]
	v_mfma_f32_16x16x32_f16 v[38:41], v[150:153], v[130:133], v[38:41]
	v_mfma_f32_16x16x32_f16 v[62:65], v[146:149], v[130:133], v[62:65]
	ds_read_b128 v[130:133], v160 offset:10240
	ds_read_b128 v[146:149], v164
	ds_read_b128 v[150:153], v164 offset:2048
	ds_read_b128 v[154:157], v164 offset:4096
	v_lshl_add_u64 v[218:219], v[218:219], 0, s[20:21]
	v_lshl_add_u64 v[222:223], v[222:223], 0, s[20:21]
	v_lshl_add_u64 v[226:227], v[226:227], 0, s[20:21]
	v_lshl_add_u64 v[220:221], v[220:221], 0, s[20:21]
	v_lshl_add_u64 v[224:225], v[224:225], 0, s[20:21]
	v_lshl_add_u64 v[228:229], v[228:229], 0, s[20:21]
	s_sub_u32 s22, s22, 1
	s_cmp_lg_u32 s22, 0
	s_cbranch_scc1 .Lgemm_T_loop
	s_waitcnt lgkmcnt(9)
	s_add_u32 m0, s11, 0x1e080
	v_mfma_f32_16x16x32_f16 v[82:85], v[134:137], v[86:89], v[82:85]
	global_load_lds_dwordx4 v[220:221], off offset:-128
	v_mfma_f32_16x16x32_f16 v[58:61], v[138:141], v[86:89], v[58:61]
	v_mfma_f32_16x16x32_f16 v[14:17], v[142:145], v[86:89], v[14:17]
	v_mfma_f32_16x16x32_f16 v[30:33], v[142:145], v[90:93], v[30:33]
	v_mfma_f32_16x16x32_f16 v[22:25], v[138:141], v[90:93], v[22:25]
	v_mfma_f32_16x16x32_f16 v[78:81], v[134:137], v[90:93], v[78:81]
	s_add_u32 m0, s11, 0x20080
	v_mfma_f32_16x16x32_f16 v[74:77], v[134:137], v[94:97], v[74:77]
	global_load_lds_dwordx4 v[224:225], off offset:-128
	v_mfma_f32_16x16x32_f16 v[18:21], v[138:141], v[94:97], v[18:21]
	v_mfma_f32_16x16x32_f16 v[26:29], v[142:145], v[94:97], v[26:29]
	v_mfma_f32_16x16x32_f16 v[240:243], v[142:145], v[98:101], v[240:243]
	v_mfma_f32_16x16x32_f16 v[46:49], v[138:141], v[98:101], v[46:49]
	v_mfma_f32_16x16x32_f16 v[70:73], v[134:137], v[98:101], v[70:73]
	s_add_u32 m0, s11, 0x22080
	v_mfma_f32_16x16x32_f16 v[66:69], v[134:137], v[102:105], v[66:69]
	global_load_lds_dwordx4 v[228:229], off offset:-128
	v_mfma_f32_16x16x32_f16 v[42:45], v[138:141], v[102:105], v[42:45]
	v_mfma_f32_16x16x32_f16 v[236:239], v[142:145], v[102:105], v[236:239]
	v_mfma_f32_16x16x32_f16 v[34:37], v[142:145], v[106:109], v[34:37]
	v_mfma_f32_16x16x32_f16 v[38:41], v[138:141], v[106:109], v[38:41]
	v_mfma_f32_16x16x32_f16 v[62:65], v[134:137], v[106:109], v[62:65]
	s_waitcnt vmcnt(6) lgkmcnt(0)
	s_barrier
	s_add_u32 m0, s11, 0x0
	ds_read_b128 v[134:137], v162 offset:49152
	global_load_lds_dwordx4 v[218:219], off
	v_mfma_f32_16x16x32_f16 v[82:85], v[146:149], v[110:113], v[82:85]
	ds_read_b128 v[138:141], v162 offset:51200
	v_mfma_f32_16x16x32_f16 v[58:61], v[150:153], v[110:113], v[58:61]
	ds_read_b128 v[142:145], v162 offset:53248
	v_mfma_f32_16x16x32_f16 v[14:17], v[154:157], v[110:113], v[14:17]
	ds_read_b128 v[86:89], v158 offset:49152
	v_mfma_f32_16x16x32_f16 v[30:33], v[154:157], v[114:117], v[30:33]
	ds_read_b128 v[90:93], v158 offset:51200
	v_mfma_f32_16x16x32_f16 v[22:25], v[150:153], v[114:117], v[22:25]
	ds_read_b128 v[94:97], v158 offset:53248
	v_mfma_f32_16x16x32_f16 v[78:81], v[146:149], v[114:117], v[78:81]
	s_add_u32 m0, s11, 0x2000
	ds_read_b128 v[98:101], v158 offset:55296
	global_load_lds_dwordx4 v[222:223], off
	v_mfma_f32_16x16x32_f16 v[74:77], v[146:149], v[118:121], v[74:77]
	ds_read_b128 v[102:105], v158 offset:57344
	v_mfma_f32_16x16x32_f16 v[18:21], v[150:153], v[118:121], v[18:21]
	ds_read_b128 v[106:109], v158 offset:59392
	v_mfma_f32_16x16x32_f16 v[26:29], v[154:157], v[118:121], v[26:29]
	ds_read_b128 v[110:113], v160 offset:49152
	v_mfma_f32_16x16x32_f16 v[240:243], v[154:157], v[122:125], v[240:243]
	ds_read_b128 v[114:117], v160 offset:51200
	v_mfma_f32_16x16x32_f16 v[46:49], v[150:153], v[122:125], v[46:49]
	v_mfma_f32_16x16x32_f16 v[70:73], v[146:149], v[122:125], v[70:73]
	s_add_u32 m0, s11, 0x4000
	ds_read_b128 v[118:121], v160 offset:53248
	global_load_lds_dwordx4 v[226:227], off
	v_mfma_f32_16x16x32_f16 v[66:69], v[146:149], v[126:129], v[66:69]
	ds_read_b128 v[122:125], v160 offset:55296
	v_mfma_f32_16x16x32_f16 v[42:45], v[150:153], v[126:129], v[42:45]
	v_mfma_f32_16x16x32_f16 v[236:239], v[154:157], v[126:129], v[236:239]
	ds_read_b128 v[126:129], v160 offset:57344
	v_mfma_f32_16x16x32_f16 v[34:37], v[154:157], v[130:133], v[34:37]
	v_mfma_f32_16x16x32_f16 v[38:41], v[150:153], v[130:133], v[38:41]
	v_mfma_f32_16x16x32_f16 v[62:65], v[146:149], v[130:133], v[62:65]
	ds_read_b128 v[130:133], v160 offset:59392
	ds_read_b128 v[146:149], v164 offset:49152
	ds_read_b128 v[150:153], v164 offset:51200
	ds_read_b128 v[154:157], v164 offset:53248
	s_waitcnt lgkmcnt(9)
	s_add_u32 m0, s11, 0x6000
	v_mfma_f32_16x16x32_f16 v[82:85], v[134:137], v[86:89], v[82:85]
	global_load_lds_dwordx4 v[220:221], off
	v_mfma_f32_16x16x32_f16 v[58:61], v[138:141], v[86:89], v[58:61]
	v_mfma_f32_16x16x32_f16 v[14:17], v[142:145], v[86:89], v[14:17]
	v_mfma_f32_16x16x32_f16 v[30:33], v[142:145], v[90:93], v[30:33]
	v_mfma_f32_16x16x32_f16 v[22:25], v[138:141], v[90:93], v[22:25]
	v_mfma_f32_16x16x32_f16 v[78:81], v[134:137], v[90:93], v[78:81]
	s_add_u32 m0, s11, 0x8000
	v_mfma_f32_16x16x32_f16 v[74:77], v[134:137], v[94:97], v[74:77]
	global_load_lds_dwordx4 v[224:225], off
	v_mfma_f32_16x16x32_f16 v[18:21], v[138:141], v[94:97], v[18:21]
	v_mfma_f32_16x16x32_f16 v[26:29], v[142:145], v[94:97], v[26:29]
	v_mfma_f32_16x16x32_f16 v[240:243], v[142:145], v[98:101], v[240:243]
	v_mfma_f32_16x16x32_f16 v[46:49], v[138:141], v[98:101], v[46:49]
	v_mfma_f32_16x16x32_f16 v[70:73], v[134:137], v[98:101], v[70:73]
	s_add_u32 m0, s11, 0xa000
	v_mfma_f32_16x16x32_f16 v[66:69], v[134:137], v[102:105], v[66:69]
	global_load_lds_dwordx4 v[228:229], off
	v_mfma_f32_16x16x32_f16 v[42:45], v[138:141], v[102:105], v[42:45]
	v_mfma_f32_16x16x32_f16 v[236:239], v[142:145], v[102:105], v[236:239]
	v_mfma_f32_16x16x32_f16 v[34:37], v[142:145], v[106:109], v[34:37]
	v_mfma_f32_16x16x32_f16 v[38:41], v[138:141], v[106:109], v[38:41]
	v_mfma_f32_16x16x32_f16 v[62:65], v[134:137], v[106:109], v[62:65]
	s_waitcnt vmcnt(6) lgkmcnt(0)
	s_barrier
	s_lshl_b32 s26, s17, 2
	s_add_u32 s26, s24, s26
	s_addc_u32 s27, s25, 0
	v_lshlrev_b32_e32 v50, 4, v231
	global_load_dwordx4 v[10:13], v50, s[26:27]
	global_load_dwordx4 v[6:9], v50, s[26:27] offset:64
	global_load_dwordx4 v[2:5], v50, s[26:27] offset:128
	ds_read_b128 v[134:137], v163
	v_mfma_f32_16x16x32_f16 v[82:85], v[146:149], v[110:113], v[82:85]
	ds_read_b128 v[138:141], v163 offset:2048
	v_mfma_f32_16x16x32_f16 v[58:61], v[150:153], v[110:113], v[58:61]
	ds_read_b128 v[142:145], v163 offset:4096
	v_mfma_f32_16x16x32_f16 v[14:17], v[154:157], v[110:113], v[14:17]
	ds_read_b128 v[86:89], v159
	v_mfma_f32_16x16x32_f16 v[30:33], v[154:157], v[114:117], v[30:33]
	ds_read_b128 v[90:93], v159 offset:2048
	v_mfma_f32_16x16x32_f16 v[22:25], v[150:153], v[114:117], v[22:25]
	ds_read_b128 v[94:97], v159 offset:4096
	v_mfma_f32_16x16x32_f16 v[78:81], v[146:149], v[114:117], v[78:81]
	ds_read_b128 v[98:101], v159 offset:6144
	v_mfma_f32_16x16x32_f16 v[74:77], v[146:149], v[118:121], v[74:77]
	ds_read_b128 v[102:105], v159 offset:8192
	v_mfma_f32_16x16x32_f16 v[18:21], v[150:153], v[118:121], v[18:21]
	ds_read_b128 v[106:109], v159 offset:10240
	v_mfma_f32_16x16x32_f16 v[26:29], v[154:157], v[118:121], v[26:29]
	ds_read_b128 v[110:113], v161
	v_mfma_f32_16x16x32_f16 v[240:243], v[154:157], v[122:125], v[240:243]
	ds_read_b128 v[114:117], v161 offset:2048
	v_mfma_f32_16x16x32_f16 v[46:49], v[150:153], v[122:125], v[46:49]
	v_mfma_f32_16x16x32_f16 v[70:73], v[146:149], v[122:125], v[70:73]
	ds_read_b128 v[118:121], v161 offset:4096
	v_mfma_f32_16x16x32_f16 v[66:69], v[146:149], v[126:129], v[66:69]
	ds_read_b128 v[122:125], v161 offset:6144
	v_mfma_f32_16x16x32_f16 v[42:45], v[150:153], v[126:129], v[42:45]
	v_mfma_f32_16x16x32_f16 v[236:239], v[154:157], v[126:129], v[236:239]
	ds_read_b128 v[126:129], v161 offset:8192
	v_mfma_f32_16x16x32_f16 v[34:37], v[154:157], v[130:133], v[34:37]
	v_mfma_f32_16x16x32_f16 v[38:41], v[150:153], v[130:133], v[38:41]
	v_mfma_f32_16x16x32_f16 v[62:65], v[146:149], v[130:133], v[62:65]
	ds_read_b128 v[130:133], v161 offset:10240
	ds_read_b128 v[146:149], v165
	ds_read_b128 v[150:153], v165 offset:2048
	ds_read_b128 v[154:157], v165 offset:4096
	s_waitcnt lgkmcnt(9)
	v_mfma_f32_16x16x32_f16 v[82:85], v[134:137], v[86:89], v[82:85]
	v_mfma_f32_16x16x32_f16 v[58:61], v[138:141], v[86:89], v[58:61]
	v_mfma_f32_16x16x32_f16 v[14:17], v[142:145], v[86:89], v[14:17]
	v_mfma_f32_16x16x32_f16 v[30:33], v[142:145], v[90:93], v[30:33]
	v_mfma_f32_16x16x32_f16 v[22:25], v[138:141], v[90:93], v[22:25]
	v_mfma_f32_16x16x32_f16 v[78:81], v[134:137], v[90:93], v[78:81]
	v_mfma_f32_16x16x32_f16 v[74:77], v[134:137], v[94:97], v[74:77]
	v_mfma_f32_16x16x32_f16 v[18:21], v[138:141], v[94:97], v[18:21]
	v_mfma_f32_16x16x32_f16 v[26:29], v[142:145], v[94:97], v[26:29]
	v_mfma_f32_16x16x32_f16 v[240:243], v[142:145], v[98:101], v[240:243]
	v_mfma_f32_16x16x32_f16 v[46:49], v[138:141], v[98:101], v[46:49]
	v_mfma_f32_16x16x32_f16 v[70:73], v[134:137], v[98:101], v[70:73]
	v_mfma_f32_16x16x32_f16 v[66:69], v[134:137], v[102:105], v[66:69]
	v_mfma_f32_16x16x32_f16 v[42:45], v[138:141], v[102:105], v[42:45]
	v_mfma_f32_16x16x32_f16 v[236:239], v[142:145], v[102:105], v[236:239]
	v_mfma_f32_16x16x32_f16 v[34:37], v[142:145], v[106:109], v[34:37]
	v_mfma_f32_16x16x32_f16 v[38:41], v[138:141], v[106:109], v[38:41]
	v_mfma_f32_16x16x32_f16 v[62:65], v[134:137], v[106:109], v[62:65]
	s_waitcnt vmcnt(3) lgkmcnt(0)
	s_barrier
	ds_read_b128 v[134:137], v162
	v_mfma_f32_16x16x32_f16 v[82:85], v[146:149], v[110:113], v[82:85]
	ds_read_b128 v[138:141], v162 offset:2048
	v_mfma_f32_16x16x32_f16 v[58:61], v[150:153], v[110:113], v[58:61]
	ds_read_b128 v[142:145], v162 offset:4096
	v_mfma_f32_16x16x32_f16 v[14:17], v[154:157], v[110:113], v[14:17]
	ds_read_b128 v[86:89], v158
	v_mfma_f32_16x16x32_f16 v[30:33], v[154:157], v[114:117], v[30:33]
	ds_read_b128 v[90:93], v158 offset:2048
	v_mfma_f32_16x16x32_f16 v[22:25], v[150:153], v[114:117], v[22:25]
	ds_read_b128 v[94:97], v158 offset:4096
	v_mfma_f32_16x16x32_f16 v[78:81], v[146:149], v[114:117], v[78:81]
	ds_read_b128 v[98:101], v158 offset:6144
	v_mfma_f32_16x16x32_f16 v[74:77], v[146:149], v[118:121], v[74:77]
	ds_read_b128 v[102:105], v158 offset:8192
	v_mfma_f32_16x16x32_f16 v[18:21], v[150:153], v[118:121], v[18:21]
	ds_read_b128 v[106:109], v158 offset:10240
	v_mfma_f32_16x16x32_f16 v[26:29], v[154:157], v[118:121], v[26:29]
	ds_read_b128 v[110:113], v160
	v_mfma_f32_16x16x32_f16 v[240:243], v[154:157], v[122:125], v[240:243]
	ds_read_b128 v[114:117], v160 offset:2048
	v_mfma_f32_16x16x32_f16 v[46:49], v[150:153], v[122:125], v[46:49]
	v_mfma_f32_16x16x32_f16 v[70:73], v[146:149], v[122:125], v[70:73]
	ds_read_b128 v[118:121], v160 offset:4096
	v_mfma_f32_16x16x32_f16 v[66:69], v[146:149], v[126:129], v[66:69]
	ds_read_b128 v[122:125], v160 offset:6144
	v_mfma_f32_16x16x32_f16 v[42:45], v[150:153], v[126:129], v[42:45]
	v_mfma_f32_16x16x32_f16 v[236:239], v[154:157], v[126:129], v[236:239]
	ds_read_b128 v[126:129], v160 offset:8192
	v_mfma_f32_16x16x32_f16 v[34:37], v[154:157], v[130:133], v[34:37]
	v_mfma_f32_16x16x32_f16 v[38:41], v[150:153], v[130:133], v[38:41]
	v_mfma_f32_16x16x32_f16 v[62:65], v[146:149], v[130:133], v[62:65]
	ds_read_b128 v[130:133], v160 offset:10240
	ds_read_b128 v[146:149], v164
	ds_read_b128 v[150:153], v164 offset:2048
	ds_read_b128 v[154:157], v164 offset:4096
	s_waitcnt lgkmcnt(9)
	v_mfma_f32_16x16x32_f16 v[82:85], v[134:137], v[86:89], v[82:85]
	v_mfma_f32_16x16x32_f16 v[58:61], v[138:141], v[86:89], v[58:61]
	v_mfma_f32_16x16x32_f16 v[14:17], v[142:145], v[86:89], v[14:17]
	v_mfma_f32_16x16x32_f16 v[30:33], v[142:145], v[90:93], v[30:33]
	v_mfma_f32_16x16x32_f16 v[22:25], v[138:141], v[90:93], v[22:25]
	v_mfma_f32_16x16x32_f16 v[78:81], v[134:137], v[90:93], v[78:81]
	v_mfma_f32_16x16x32_f16 v[74:77], v[134:137], v[94:97], v[74:77]
	v_mfma_f32_16x16x32_f16 v[18:21], v[138:141], v[94:97], v[18:21]
	v_mfma_f32_16x16x32_f16 v[26:29], v[142:145], v[94:97], v[26:29]
	v_mfma_f32_16x16x32_f16 v[240:243], v[142:145], v[98:101], v[240:243]
	v_mfma_f32_16x16x32_f16 v[46:49], v[138:141], v[98:101], v[46:49]
	v_mfma_f32_16x16x32_f16 v[70:73], v[134:137], v[98:101], v[70:73]
	v_mfma_f32_16x16x32_f16 v[66:69], v[134:137], v[102:105], v[66:69]
	v_mfma_f32_16x16x32_f16 v[42:45], v[138:141], v[102:105], v[42:45]
	v_mfma_f32_16x16x32_f16 v[236:239], v[142:145], v[102:105], v[236:239]
	v_mfma_f32_16x16x32_f16 v[34:37], v[142:145], v[106:109], v[34:37]
	v_mfma_f32_16x16x32_f16 v[38:41], v[138:141], v[106:109], v[38:41]
	v_mfma_f32_16x16x32_f16 v[62:65], v[134:137], v[106:109], v[62:65]
	s_waitcnt lgkmcnt(0)
	v_mfma_f32_16x16x32_f16 v[82:85], v[146:149], v[110:113], v[82:85]
	v_mfma_f32_16x16x32_f16 v[58:61], v[150:153], v[110:113], v[58:61]
	v_mfma_f32_16x16x32_f16 v[14:17], v[154:157], v[110:113], v[14:17]
	v_mfma_f32_16x16x32_f16 v[30:33], v[154:157], v[114:117], v[30:33]
	v_mfma_f32_16x16x32_f16 v[22:25], v[150:153], v[114:117], v[22:25]
	v_mfma_f32_16x16x32_f16 v[78:81], v[146:149], v[114:117], v[78:81]
	v_mfma_f32_16x16x32_f16 v[74:77], v[146:149], v[118:121], v[74:77]
	v_mfma_f32_16x16x32_f16 v[18:21], v[150:153], v[118:121], v[18:21]
	v_mfma_f32_16x16x32_f16 v[26:29], v[154:157], v[118:121], v[26:29]
	v_mfma_f32_16x16x32_f16 v[240:243], v[154:157], v[122:125], v[240:243]
	v_mfma_f32_16x16x32_f16 v[46:49], v[150:153], v[122:125], v[46:49]
	v_mfma_f32_16x16x32_f16 v[70:73], v[146:149], v[122:125], v[70:73]
	v_mfma_f32_16x16x32_f16 v[66:69], v[146:149], v[126:129], v[66:69]
	v_mfma_f32_16x16x32_f16 v[42:45], v[150:153], v[126:129], v[42:45]
	v_mfma_f32_16x16x32_f16 v[236:239], v[154:157], v[126:129], v[236:239]
	v_mfma_f32_16x16x32_f16 v[34:37], v[154:157], v[130:133], v[34:37]
	v_mfma_f32_16x16x32_f16 v[38:41], v[150:153], v[130:133], v[38:41]
	v_mfma_f32_16x16x32_f16 v[62:65], v[146:149], v[130:133], v[62:65]
	s_branch .LBB1_76
.Lgemm_N_loop:
	s_waitcnt lgkmcnt(9)
	s_add_u32 m0, s11, 0x1e080
	v_mfma_f32_16x16x32_f16 v[82:85], v[86:89], v[134:137], v[82:85]
	global_load_lds_dwordx4 v[220:221], off offset:-128
	v_mfma_f32_16x16x32_f16 v[58:61], v[86:89], v[138:141], v[58:61]
	v_mfma_f32_16x16x32_f16 v[14:17], v[86:89], v[142:145], v[14:17]
	v_mfma_f32_16x16x32_f16 v[30:33], v[90:93], v[142:145], v[30:33]
	v_mfma_f32_16x16x32_f16 v[22:25], v[90:93], v[138:141], v[22:25]
	v_mfma_f32_16x16x32_f16 v[78:81], v[90:93], v[134:137], v[78:81]
	s_add_u32 m0, s11, 0x20080
	v_mfma_f32_16x16x32_f16 v[74:77], v[94:97], v[134:137], v[74:77]
	global_load_lds_dwordx4 v[224:225], off offset:-128
	v_mfma_f32_16x16x32_f16 v[18:21], v[94:97], v[138:141], v[18:21]
	v_mfma_f32_16x16x32_f16 v[26:29], v[94:97], v[142:145], v[26:29]
	v_mfma_f32_16x16x32_f16 v[240:243], v[98:101], v[142:145], v[240:243]
	v_mfma_f32_16x16x32_f16 v[46:49], v[98:101], v[138:141], v[46:49]
	v_mfma_f32_16x16x32_f16 v[70:73], v[98:101], v[134:137], v[70:73]
	s_add_u32 m0, s11, 0x22080
	v_mfma_f32_16x16x32_f16 v[66:69], v[102:105], v[134:137], v[66:69]
	global_load_lds_dwordx4 v[228:229], off offset:-128
	v_mfma_f32_16x16x32_f16 v[42:45], v[102:105], v[138:141], v[42:45]
	v_mfma_f32_16x16x32_f16 v[236:239], v[102:105], v[142:145], v[236:239]
	v_mfma_f32_16x16x32_f16 v[34:37], v[106:109], v[142:145], v[34:37]
	v_mfma_f32_16x16x32_f16 v[38:41], v[106:109], v[138:141], v[38:41]
	v_mfma_f32_16x16x32_f16 v[62:65], v[106:109], v[134:137], v[62:65]
	s_waitcnt vmcnt(6) lgkmcnt(0)
	s_barrier
	s_add_u32 m0, s11, 0x0
	ds_read_b128 v[134:137], v162 offset:49152
	global_load_lds_dwordx4 v[218:219], off
	v_mfma_f32_16x16x32_f16 v[82:85], v[110:113], v[146:149], v[82:85]
	ds_read_b128 v[138:141], v162 offset:51200
	v_mfma_f32_16x16x32_f16 v[58:61], v[110:113], v[150:153], v[58:61]
	ds_read_b128 v[142:145], v162 offset:53248
	v_mfma_f32_16x16x32_f16 v[14:17], v[110:113], v[154:157], v[14:17]
	ds_read_b128 v[86:89], v158 offset:49152
	v_mfma_f32_16x16x32_f16 v[30:33], v[114:117], v[154:157], v[30:33]
	ds_read_b128 v[90:93], v158 offset:51200
	v_mfma_f32_16x16x32_f16 v[22:25], v[114:117], v[150:153], v[22:25]
	ds_read_b128 v[94:97], v158 offset:53248
	v_mfma_f32_16x16x32_f16 v[78:81], v[114:117], v[146:149], v[78:81]
	s_add_u32 m0, s11, 0x2000
	ds_read_b128 v[98:101], v158 offset:55296
	global_load_lds_dwordx4 v[222:223], off
	v_mfma_f32_16x16x32_f16 v[74:77], v[118:121], v[146:149], v[74:77]
	ds_read_b128 v[102:105], v158 offset:57344
	v_mfma_f32_16x16x32_f16 v[18:21], v[118:121], v[150:153], v[18:21]
	ds_read_b128 v[106:109], v158 offset:59392
	v_mfma_f32_16x16x32_f16 v[26:29], v[118:121], v[154:157], v[26:29]
	ds_read_b128 v[110:113], v160 offset:49152
	v_mfma_f32_16x16x32_f16 v[240:243], v[122:125], v[154:157], v[240:243]
	ds_read_b128 v[114:117], v160 offset:51200
	v_mfma_f32_16x16x32_f16 v[46:49], v[122:125], v[150:153], v[46:49]
	v_mfma_f32_16x16x32_f16 v[70:73], v[122:125], v[146:149], v[70:73]
	s_add_u32 m0, s11, 0x4000
	ds_read_b128 v[118:121], v160 offset:53248
	global_load_lds_dwordx4 v[226:227], off
	v_mfma_f32_16x16x32_f16 v[66:69], v[126:129], v[146:149], v[66:69]
	ds_read_b128 v[122:125], v160 offset:55296
	v_mfma_f32_16x16x32_f16 v[42:45], v[126:129], v[150:153], v[42:45]
	v_mfma_f32_16x16x32_f16 v[236:239], v[126:129], v[154:157], v[236:239]
	ds_read_b128 v[126:129], v160 offset:57344
	v_mfma_f32_16x16x32_f16 v[34:37], v[130:133], v[154:157], v[34:37]
	v_mfma_f32_16x16x32_f16 v[38:41], v[130:133], v[150:153], v[38:41]
	v_mfma_f32_16x16x32_f16 v[62:65], v[130:133], v[146:149], v[62:65]
	ds_read_b128 v[130:133], v160 offset:59392
	ds_read_b128 v[146:149], v164 offset:49152
	ds_read_b128 v[150:153], v164 offset:51200
	ds_read_b128 v[154:157], v164 offset:53248
	s_waitcnt lgkmcnt(9)
	s_add_u32 m0, s11, 0x6000
	v_mfma_f32_16x16x32_f16 v[82:85], v[86:89], v[134:137], v[82:85]
	global_load_lds_dwordx4 v[220:221], off
	v_mfma_f32_16x16x32_f16 v[58:61], v[86:89], v[138:141], v[58:61]
	v_mfma_f32_16x16x32_f16 v[14:17], v[86:89], v[142:145], v[14:17]
	v_mfma_f32_16x16x32_f16 v[30:33], v[90:93], v[142:145], v[30:33]
	v_mfma_f32_16x16x32_f16 v[22:25], v[90:93], v[138:141], v[22:25]
	v_mfma_f32_16x16x32_f16 v[78:81], v[90:93], v[134:137], v[78:81]
	s_add_u32 m0, s11, 0x8000
	v_mfma_f32_16x16x32_f16 v[74:77], v[94:97], v[134:137], v[74:77]
	global_load_lds_dwordx4 v[224:225], off
	v_mfma_f32_16x16x32_f16 v[18:21], v[94:97], v[138:141], v[18:21]
	v_mfma_f32_16x16x32_f16 v[26:29], v[94:97], v[142:145], v[26:29]
	v_mfma_f32_16x16x32_f16 v[240:243], v[98:101], v[142:145], v[240:243]
	v_mfma_f32_16x16x32_f16 v[46:49], v[98:101], v[138:141], v[46:49]
	v_mfma_f32_16x16x32_f16 v[70:73], v[98:101], v[134:137], v[70:73]
	s_add_u32 m0, s11, 0xa000
	v_mfma_f32_16x16x32_f16 v[66:69], v[102:105], v[134:137], v[66:69]
	global_load_lds_dwordx4 v[228:229], off
	v_mfma_f32_16x16x32_f16 v[42:45], v[102:105], v[138:141], v[42:45]
	v_mfma_f32_16x16x32_f16 v[236:239], v[102:105], v[142:145], v[236:239]
	v_mfma_f32_16x16x32_f16 v[34:37], v[106:109], v[142:145], v[34:37]
	v_mfma_f32_16x16x32_f16 v[38:41], v[106:109], v[138:141], v[38:41]
	v_mfma_f32_16x16x32_f16 v[62:65], v[106:109], v[134:137], v[62:65]
	s_waitcnt vmcnt(6) lgkmcnt(0)
	s_barrier
	s_add_u32 m0, s11, 0xbf80
	ds_read_b128 v[134:137], v163
	global_load_lds_dwordx4 v[218:219], off offset:128
	v_mfma_f32_16x16x32_f16 v[82:85], v[110:113], v[146:149], v[82:85]
	ds_read_b128 v[138:141], v163 offset:2048
	v_mfma_f32_16x16x32_f16 v[58:61], v[110:113], v[150:153], v[58:61]
	ds_read_b128 v[142:145], v163 offset:4096
	v_mfma_f32_16x16x32_f16 v[14:17], v[110:113], v[154:157], v[14:17]
	ds_read_b128 v[86:89], v159
	v_mfma_f32_16x16x32_f16 v[30:33], v[114:117], v[154:157], v[30:33]
	ds_read_b128 v[90:93], v159 offset:2048
	v_mfma_f32_16x16x32_f16 v[22:25], v[114:117], v[150:153], v[22:25]
	ds_read_b128 v[94:97], v159 offset:4096
	v_mfma_f32_16x16x32_f16 v[78:81], v[114:117], v[146:149], v[78:81]
	s_add_u32 m0, s11, 0xdf80
	ds_read_b128 v[98:101], v159 offset:6144
	global_load_lds_dwordx4 v[222:223], off offset:128
	v_mfma_f32_16x16x32_f16 v[74:77], v[118:121], v[146:149], v[74:77]
	ds_read_b128 v[102:105], v159 offset:8192
	v_mfma_f32_16x16x32_f16 v[18:21], v[118:121], v[150:153], v[18:21]
	ds_read_b128 v[106:109], v159 offset:10240
	v_mfma_f32_16x16x32_f16 v[26:29], v[118:121], v[154:157], v[26:29]
	ds_read_b128 v[110:113], v161
	v_mfma_f32_16x16x32_f16 v[240:243], v[122:125], v[154:157], v[240:243]
	ds_read_b128 v[114:117], v161 offset:2048
	v_mfma_f32_16x16x32_f16 v[46:49], v[122:125], v[150:153], v[46:49]
	v_mfma_f32_16x16x32_f16 v[70:73], v[122:125], v[146:149], v[70:73]
	s_add_u32 m0, s11, 0xff80
	ds_read_b128 v[118:121], v161 offset:4096
	global_load_lds_dwordx4 v[226:227], off offset:128
	v_mfma_f32_16x16x32_f16 v[66:69], v[126:129], v[146:149], v[66:69]
	ds_read_b128 v[122:125], v161 offset:6144
	v_mfma_f32_16x16x32_f16 v[42:45], v[126:129], v[150:153], v[42:45]
	v_mfma_f32_16x16x32_f16 v[236:239], v[126:129], v[154:157], v[236:239]
	ds_read_b128 v[126:129], v161 offset:8192
	v_mfma_f32_16x16x32_f16 v[34:37], v[130:133], v[154:157], v[34:37]
	v_mfma_f32_16x16x32_f16 v[38:41], v[130:133], v[150:153], v[38:41]
	v_mfma_f32_16x16x32_f16 v[62:65], v[130:133], v[146:149], v[62:65]
	ds_read_b128 v[130:133], v161 offset:10240
	ds_read_b128 v[146:149], v165
	ds_read_b128 v[150:153], v165 offset:2048
	ds_read_b128 v[154:157], v165 offset:4096
	s_waitcnt lgkmcnt(9)
	s_add_u32 m0, s11, 0x11f80
	v_mfma_f32_16x16x32_f16 v[82:85], v[86:89], v[134:137], v[82:85]
	global_load_lds_dwordx4 v[220:221], off offset:128
	v_mfma_f32_16x16x32_f16 v[58:61], v[86:89], v[138:141], v[58:61]
	v_mfma_f32_16x16x32_f16 v[14:17], v[86:89], v[142:145], v[14:17]
	v_mfma_f32_16x16x32_f16 v[30:33], v[90:93], v[142:145], v[30:33]
	v_mfma_f32_16x16x32_f16 v[22:25], v[90:93], v[138:141], v[22:25]
	v_mfma_f32_16x16x32_f16 v[78:81], v[90:93], v[134:137], v[78:81]
	s_add_u32 m0, s11, 0x13f80
	v_mfma_f32_16x16x32_f16 v[74:77], v[94:97], v[134:137], v[74:77]
	global_load_lds_dwordx4 v[224:225], off offset:128
	v_mfma_f32_16x16x32_f16 v[18:21], v[94:97], v[138:141], v[18:21]
	v_mfma_f32_16x16x32_f16 v[26:29], v[94:97], v[142:145], v[26:29]
	v_mfma_f32_16x16x32_f16 v[240:243], v[98:101], v[142:145], v[240:243]
	v_mfma_f32_16x16x32_f16 v[46:49], v[98:101], v[138:141], v[46:49]
	v_mfma_f32_16x16x32_f16 v[70:73], v[98:101], v[134:137], v[70:73]
	s_add_u32 m0, s11, 0x15f80
	v_mfma_f32_16x16x32_f16 v[66:69], v[102:105], v[134:137], v[66:69]
	global_load_lds_dwordx4 v[228:229], off offset:128
	v_mfma_f32_16x16x32_f16 v[42:45], v[102:105], v[138:141], v[42:45]
	v_mfma_f32_16x16x32_f16 v[236:239], v[102:105], v[142:145], v[236:239]
	v_mfma_f32_16x16x32_f16 v[34:37], v[106:109], v[142:145], v[34:37]
	v_mfma_f32_16x16x32_f16 v[38:41], v[106:109], v[138:141], v[38:41]
	v_mfma_f32_16x16x32_f16 v[62:65], v[106:109], v[134:137], v[62:65]
	s_waitcnt vmcnt(6) lgkmcnt(0)
	s_barrier
	s_add_u32 m0, s11, 0x17f00
	ds_read_b128 v[134:137], v162
	global_load_lds_dwordx4 v[218:219], off offset:256
	v_mfma_f32_16x16x32_f16 v[82:85], v[110:113], v[146:149], v[82:85]
	ds_read_b128 v[138:141], v162 offset:2048
	v_mfma_f32_16x16x32_f16 v[58:61], v[110:113], v[150:153], v[58:61]
	ds_read_b128 v[142:145], v162 offset:4096
	v_mfma_f32_16x16x32_f16 v[14:17], v[110:113], v[154:157], v[14:17]
	ds_read_b128 v[86:89], v158
	v_mfma_f32_16x16x32_f16 v[30:33], v[114:117], v[154:157], v[30:33]
	ds_read_b128 v[90:93], v158 offset:2048
	v_mfma_f32_16x16x32_f16 v[22:25], v[114:117], v[150:153], v[22:25]
	ds_read_b128 v[94:97], v158 offset:4096
	v_mfma_f32_16x16x32_f16 v[78:81], v[114:117], v[146:149], v[78:81]
	s_add_u32 m0, s11, 0x19f00
	ds_read_b128 v[98:101], v158 offset:6144
	global_load_lds_dwordx4 v[222:223], off offset:256
	v_mfma_f32_16x16x32_f16 v[74:77], v[118:121], v[146:149], v[74:77]
	ds_read_b128 v[102:105], v158 offset:8192
	v_mfma_f32_16x16x32_f16 v[18:21], v[118:121], v[150:153], v[18:21]
	ds_read_b128 v[106:109], v158 offset:10240
	v_mfma_f32_16x16x32_f16 v[26:29], v[118:121], v[154:157], v[26:29]
	ds_read_b128 v[110:113], v160
	v_mfma_f32_16x16x32_f16 v[240:243], v[122:125], v[154:157], v[240:243]
	ds_read_b128 v[114:117], v160 offset:2048
	v_mfma_f32_16x16x32_f16 v[46:49], v[122:125], v[150:153], v[46:49]
	v_mfma_f32_16x16x32_f16 v[70:73], v[122:125], v[146:149], v[70:73]
	s_add_u32 m0, s11, 0x1bf00
	ds_read_b128 v[118:121], v160 offset:4096
	global_load_lds_dwordx4 v[226:227], off offset:256
	v_mfma_f32_16x16x32_f16 v[66:69], v[126:129], v[146:149], v[66:69]
	ds_read_b128 v[122:125], v160 offset:6144
	v_mfma_f32_16x16x32_f16 v[42:45], v[126:129], v[150:153], v[42:45]
	v_mfma_f32_16x16x32_f16 v[236:239], v[126:129], v[154:157], v[236:239]
	ds_read_b128 v[126:129], v160 offset:8192
	v_mfma_f32_16x16x32_f16 v[34:37], v[130:133], v[154:157], v[34:37]
	v_mfma_f32_16x16x32_f16 v[38:41], v[130:133], v[150:153], v[38:41]
	v_mfma_f32_16x16x32_f16 v[62:65], v[130:133], v[146:149], v[62:65]
	ds_read_b128 v[130:133], v160 offset:10240
	ds_read_b128 v[146:149], v164
	ds_read_b128 v[150:153], v164 offset:2048
	ds_read_b128 v[154:157], v164 offset:4096
	v_lshl_add_u64 v[218:219], v[218:219], 0, s[20:21]
	v_lshl_add_u64 v[222:223], v[222:223], 0, s[20:21]
	v_lshl_add_u64 v[226:227], v[226:227], 0, s[20:21]
	v_lshl_add_u64 v[220:221], v[220:221], 0, s[20:21]
	v_lshl_add_u64 v[224:225], v[224:225], 0, s[20:21]
	v_lshl_add_u64 v[228:229], v[228:229], 0, s[20:21]
	s_sub_u32 s22, s22, 1
	s_cmp_lg_u32 s22, 0
	s_cbranch_scc1 .Lgemm_N_loop
	s_waitcnt lgkmcnt(9)
	s_add_u32 m0, s11, 0x1e080
	v_mfma_f32_16x16x32_f16 v[82:85], v[86:89], v[134:137], v[82:85]
	global_load_lds_dwordx4 v[220:221], off offset:-128
	v_mfma_f32_16x16x32_f16 v[58:61], v[86:89], v[138:141], v[58:61]
	v_mfma_f32_16x16x32_f16 v[14:17], v[86:89], v[142:145], v[14:17]
	v_mfma_f32_16x16x32_f16 v[30:33], v[90:93], v[142:145], v[30:33]
	v_mfma_f32_16x16x32_f16 v[22:25], v[90:93], v[138:141], v[22:25]
	v_mfma_f32_16x16x32_f16 v[78:81], v[90:93], v[134:137], v[78:81]
	s_add_u32 m0, s11, 0x20080
	v_mfma_f32_16x16x32_f16 v[74:77], v[94:97], v[134:137], v[74:77]
	global_load_lds_dwordx4 v[224:225], off offset:-128
	v_mfma_f32_16x16x32_f16 v[18:21], v[94:97], v[138:141], v[18:21]
	v_mfma_f32_16x16x32_f16 v[26:29], v[94:97], v[142:145], v[26:29]
	v_mfma_f32_16x16x32_f16 v[240:243], v[98:101], v[142:145], v[240:243]
	v_mfma_f32_16x16x32_f16 v[46:49], v[98:101], v[138:141], v[46:49]
	v_mfma_f32_16x16x32_f16 v[70:73], v[98:101], v[134:137], v[70:73]
	s_add_u32 m0, s11, 0x22080
	v_mfma_f32_16x16x32_f16 v[66:69], v[102:105], v[134:137], v[66:69]
	global_load_lds_dwordx4 v[228:229], off offset:-128
	v_mfma_f32_16x16x32_f16 v[42:45], v[102:105], v[138:141], v[42:45]
	v_mfma_f32_16x16x32_f16 v[236:239], v[102:105], v[142:145], v[236:239]
	v_mfma_f32_16x16x32_f16 v[34:37], v[106:109], v[142:145], v[34:37]
	v_mfma_f32_16x16x32_f16 v[38:41], v[106:109], v[138:141], v[38:41]
	v_mfma_f32_16x16x32_f16 v[62:65], v[106:109], v[134:137], v[62:65]
	s_waitcnt vmcnt(6) lgkmcnt(0)
	s_barrier
	s_add_u32 m0, s11, 0x0
	ds_read_b128 v[134:137], v162 offset:49152
	global_load_lds_dwordx4 v[218:219], off
	v_mfma_f32_16x16x32_f16 v[82:85], v[110:113], v[146:149], v[82:85]
	ds_read_b128 v[138:141], v162 offset:51200
	v_mfma_f32_16x16x32_f16 v[58:61], v[110:113], v[150:153], v[58:61]
	ds_read_b128 v[142:145], v162 offset:53248
	v_mfma_f32_16x16x32_f16 v[14:17], v[110:113], v[154:157], v[14:17]
	ds_read_b128 v[86:89], v158 offset:49152
	v_mfma_f32_16x16x32_f16 v[30:33], v[114:117], v[154:157], v[30:33]
	ds_read_b128 v[90:93], v158 offset:51200
	v_mfma_f32_16x16x32_f16 v[22:25], v[114:117], v[150:153], v[22:25]
	ds_read_b128 v[94:97], v158 offset:53248
	v_mfma_f32_16x16x32_f16 v[78:81], v[114:117], v[146:149], v[78:81]
	s_add_u32 m0, s11, 0x2000
	ds_read_b128 v[98:101], v158 offset:55296
	global_load_lds_dwordx4 v[222:223], off
	v_mfma_f32_16x16x32_f16 v[74:77], v[118:121], v[146:149], v[74:77]
	ds_read_b128 v[102:105], v158 offset:57344
	v_mfma_f32_16x16x32_f16 v[18:21], v[118:121], v[150:153], v[18:21]
	ds_read_b128 v[106:109], v158 offset:59392
	v_mfma_f32_16x16x32_f16 v[26:29], v[118:121], v[154:157], v[26:29]
	ds_read_b128 v[110:113], v160 offset:49152
	v_mfma_f32_16x16x32_f16 v[240:243], v[122:125], v[154:157], v[240:243]
	ds_read_b128 v[114:117], v160 offset:51200
	v_mfma_f32_16x16x32_f16 v[46:49], v[122:125], v[150:153], v[46:49]
	v_mfma_f32_16x16x32_f16 v[70:73], v[122:125], v[146:149], v[70:73]
	s_add_u32 m0, s11, 0x4000
	ds_read_b128 v[118:121], v160 offset:53248
	global_load_lds_dwordx4 v[226:227], off
	v_mfma_f32_16x16x32_f16 v[66:69], v[126:129], v[146:149], v[66:69]
	ds_read_b128 v[122:125], v160 offset:55296
	v_mfma_f32_16x16x32_f16 v[42:45], v[126:129], v[150:153], v[42:45]
	v_mfma_f32_16x16x32_f16 v[236:239], v[126:129], v[154:157], v[236:239]
	ds_read_b128 v[126:129], v160 offset:57344
	v_mfma_f32_16x16x32_f16 v[34:37], v[130:133], v[154:157], v[34:37]
	v_mfma_f32_16x16x32_f16 v[38:41], v[130:133], v[150:153], v[38:41]
	v_mfma_f32_16x16x32_f16 v[62:65], v[130:133], v[146:149], v[62:65]
	ds_read_b128 v[130:133], v160 offset:59392
	ds_read_b128 v[146:149], v164 offset:49152
	ds_read_b128 v[150:153], v164 offset:51200
	ds_read_b128 v[154:157], v164 offset:53248
	s_waitcnt lgkmcnt(9)
	s_add_u32 m0, s11, 0x6000
	v_mfma_f32_16x16x32_f16 v[82:85], v[86:89], v[134:137], v[82:85]
	global_load_lds_dwordx4 v[220:221], off
	v_mfma_f32_16x16x32_f16 v[58:61], v[86:89], v[138:141], v[58:61]
	v_mfma_f32_16x16x32_f16 v[14:17], v[86:89], v[142:145], v[14:17]
	v_mfma_f32_16x16x32_f16 v[30:33], v[90:93], v[142:145], v[30:33]
	v_mfma_f32_16x16x32_f16 v[22:25], v[90:93], v[138:141], v[22:25]
	v_mfma_f32_16x16x32_f16 v[78:81], v[90:93], v[134:137], v[78:81]
	s_add_u32 m0, s11, 0x8000
	v_mfma_f32_16x16x32_f16 v[74:77], v[94:97], v[134:137], v[74:77]
	global_load_lds_dwordx4 v[224:225], off
	v_mfma_f32_16x16x32_f16 v[18:21], v[94:97], v[138:141], v[18:21]
	v_mfma_f32_16x16x32_f16 v[26:29], v[94:97], v[142:145], v[26:29]
	v_mfma_f32_16x16x32_f16 v[240:243], v[98:101], v[142:145], v[240:243]
	v_mfma_f32_16x16x32_f16 v[46:49], v[98:101], v[138:141], v[46:49]
	v_mfma_f32_16x16x32_f16 v[70:73], v[98:101], v[134:137], v[70:73]
	s_add_u32 m0, s11, 0xa000
	v_mfma_f32_16x16x32_f16 v[66:69], v[102:105], v[134:137], v[66:69]
	global_load_lds_dwordx4 v[228:229], off
	v_mfma_f32_16x16x32_f16 v[42:45], v[102:105], v[138:141], v[42:45]
	v_mfma_f32_16x16x32_f16 v[236:239], v[102:105], v[142:145], v[236:239]
	v_mfma_f32_16x16x32_f16 v[34:37], v[106:109], v[142:145], v[34:37]
	v_mfma_f32_16x16x32_f16 v[38:41], v[106:109], v[138:141], v[38:41]
	v_mfma_f32_16x16x32_f16 v[62:65], v[106:109], v[134:137], v[62:65]
	s_waitcnt vmcnt(6) lgkmcnt(0)
	s_barrier
	s_lshl_b32 s26, s17, 2
	s_add_u32 s26, s24, s26
	s_addc_u32 s27, s25, 0
	v_lshlrev_b32_e32 v50, 2, v1
	global_load_dword v234, v50, s[26:27]
	global_load_dword v232, v50, s[26:27] offset:64
	global_load_dword v230, v50, s[26:27] offset:128
	ds_read_b128 v[134:137], v163
	v_mfma_f32_16x16x32_f16 v[82:85], v[110:113], v[146:149], v[82:85]
	ds_read_b128 v[138:141], v163 offset:2048
	v_mfma_f32_16x16x32_f16 v[58:61], v[110:113], v[150:153], v[58:61]
	ds_read_b128 v[142:145], v163 offset:4096
	v_mfma_f32_16x16x32_f16 v[14:17], v[110:113], v[154:157], v[14:17]
	ds_read_b128 v[86:89], v159
	v_mfma_f32_16x16x32_f16 v[30:33], v[114:117], v[154:157], v[30:33]
	ds_read_b128 v[90:93], v159 offset:2048
	v_mfma_f32_16x16x32_f16 v[22:25], v[114:117], v[150:153], v[22:25]
	ds_read_b128 v[94:97], v159 offset:4096
	v_mfma_f32_16x16x32_f16 v[78:81], v[114:117], v[146:149], v[78:81]
	ds_read_b128 v[98:101], v159 offset:6144
	v_mfma_f32_16x16x32_f16 v[74:77], v[118:121], v[146:149], v[74:77]
	ds_read_b128 v[102:105], v159 offset:8192
	v_mfma_f32_16x16x32_f16 v[18:21], v[118:121], v[150:153], v[18:21]
	ds_read_b128 v[106:109], v159 offset:10240
	v_mfma_f32_16x16x32_f16 v[26:29], v[118:121], v[154:157], v[26:29]
	ds_read_b128 v[110:113], v161
	v_mfma_f32_16x16x32_f16 v[240:243], v[122:125], v[154:157], v[240:243]
	ds_read_b128 v[114:117], v161 offset:2048
	v_mfma_f32_16x16x32_f16 v[46:49], v[122:125], v[150:153], v[46:49]
	v_mfma_f32_16x16x32_f16 v[70:73], v[122:125], v[146:149], v[70:73]
	ds_read_b128 v[118:121], v161 offset:4096
	v_mfma_f32_16x16x32_f16 v[66:69], v[126:129], v[146:149], v[66:69]
	ds_read_b128 v[122:125], v161 offset:6144
	v_mfma_f32_16x16x32_f16 v[42:45], v[126:129], v[150:153], v[42:45]
	v_mfma_f32_16x16x32_f16 v[236:239], v[126:129], v[154:157], v[236:239]
	ds_read_b128 v[126:129], v161 offset:8192
	v_mfma_f32_16x16x32_f16 v[34:37], v[130:133], v[154:157], v[34:37]
	v_mfma_f32_16x16x32_f16 v[38:41], v[130:133], v[150:153], v[38:41]
	v_mfma_f32_16x16x32_f16 v[62:65], v[130:133], v[146:149], v[62:65]
	ds_read_b128 v[130:133], v161 offset:10240
	ds_read_b128 v[146:149], v165
	ds_read_b128 v[150:153], v165 offset:2048
	ds_read_b128 v[154:157], v165 offset:4096
	s_waitcnt lgkmcnt(9)
	v_mfma_f32_16x16x32_f16 v[82:85], v[86:89], v[134:137], v[82:85]
	v_mfma_f32_16x16x32_f16 v[58:61], v[86:89], v[138:141], v[58:61]
	v_mfma_f32_16x16x32_f16 v[14:17], v[86:89], v[142:145], v[14:17]
	v_mfma_f32_16x16x32_f16 v[30:33], v[90:93], v[142:145], v[30:33]
	v_mfma_f32_16x16x32_f16 v[22:25], v[90:93], v[138:141], v[22:25]
	v_mfma_f32_16x16x32_f16 v[78:81], v[90:93], v[134:137], v[78:81]
	v_mfma_f32_16x16x32_f16 v[74:77], v[94:97], v[134:137], v[74:77]
	v_mfma_f32_16x16x32_f16 v[18:21], v[94:97], v[138:141], v[18:21]
	v_mfma_f32_16x16x32_f16 v[26:29], v[94:97], v[142:145], v[26:29]
	v_mfma_f32_16x16x32_f16 v[240:243], v[98:101], v[142:145], v[240:243]
	v_mfma_f32_16x16x32_f16 v[46:49], v[98:101], v[138:141], v[46:49]
	v_mfma_f32_16x16x32_f16 v[70:73], v[98:101], v[134:137], v[70:73]
	v_mfma_f32_16x16x32_f16 v[66:69], v[102:105], v[134:137], v[66:69]
	v_mfma_f32_16x16x32_f16 v[42:45], v[102:105], v[138:141], v[42:45]
	v_mfma_f32_16x16x32_f16 v[236:239], v[102:105], v[142:145], v[236:239]
	v_mfma_f32_16x16x32_f16 v[34:37], v[106:109], v[142:145], v[34:37]
	v_mfma_f32_16x16x32_f16 v[38:41], v[106:109], v[138:141], v[38:41]
	v_mfma_f32_16x16x32_f16 v[62:65], v[106:109], v[134:137], v[62:65]
	s_waitcnt vmcnt(3) lgkmcnt(0)
	s_barrier
	ds_read_b128 v[134:137], v162
	v_mfma_f32_16x16x32_f16 v[82:85], v[110:113], v[146:149], v[82:85]
	ds_read_b128 v[138:141], v162 offset:2048
	v_mfma_f32_16x16x32_f16 v[58:61], v[110:113], v[150:153], v[58:61]
	ds_read_b128 v[142:145], v162 offset:4096
	v_mfma_f32_16x16x32_f16 v[14:17], v[110:113], v[154:157], v[14:17]
	ds_read_b128 v[86:89], v158
	v_mfma_f32_16x16x32_f16 v[30:33], v[114:117], v[154:157], v[30:33]
	ds_read_b128 v[90:93], v158 offset:2048
	v_mfma_f32_16x16x32_f16 v[22:25], v[114:117], v[150:153], v[22:25]
	ds_read_b128 v[94:97], v158 offset:4096
	v_mfma_f32_16x16x32_f16 v[78:81], v[114:117], v[146:149], v[78:81]
	ds_read_b128 v[98:101], v158 offset:6144
	v_mfma_f32_16x16x32_f16 v[74:77], v[118:121], v[146:149], v[74:77]
	ds_read_b128 v[102:105], v158 offset:8192
	v_mfma_f32_16x16x32_f16 v[18:21], v[118:121], v[150:153], v[18:21]
	ds_read_b128 v[106:109], v158 offset:10240
	v_mfma_f32_16x16x32_f16 v[26:29], v[118:121], v[154:157], v[26:29]
	ds_read_b128 v[110:113], v160
	v_mfma_f32_16x16x32_f16 v[240:243], v[122:125], v[154:157], v[240:243]
	ds_read_b128 v[114:117], v160 offset:2048
	v_mfma_f32_16x16x32_f16 v[46:49], v[122:125], v[150:153], v[46:49]
	v_mfma_f32_16x16x32_f16 v[70:73], v[122:125], v[146:149], v[70:73]
	ds_read_b128 v[118:121], v160 offset:4096
	v_mfma_f32_16x16x32_f16 v[66:69], v[126:129], v[146:149], v[66:69]
	ds_read_b128 v[122:125], v160 offset:6144
	v_mfma_f32_16x16x32_f16 v[42:45], v[126:129], v[150:153], v[42:45]
	v_mfma_f32_16x16x32_f16 v[236:239], v[126:129], v[154:157], v[236:239]
	ds_read_b128 v[126:129], v160 offset:8192
	v_mfma_f32_16x16x32_f16 v[34:37], v[130:133], v[154:157], v[34:37]
	v_mfma_f32_16x16x32_f16 v[38:41], v[130:133], v[150:153], v[38:41]
	v_mfma_f32_16x16x32_f16 v[62:65], v[130:133], v[146:149], v[62:65]
	ds_read_b128 v[130:133], v160 offset:10240
	ds_read_b128 v[146:149], v164
	ds_read_b128 v[150:153], v164 offset:2048
	ds_read_b128 v[154:157], v164 offset:4096
	s_waitcnt lgkmcnt(9)
	v_mfma_f32_16x16x32_f16 v[82:85], v[86:89], v[134:137], v[82:85]
	v_mfma_f32_16x16x32_f16 v[58:61], v[86:89], v[138:141], v[58:61]
	v_mfma_f32_16x16x32_f16 v[14:17], v[86:89], v[142:145], v[14:17]
	v_mfma_f32_16x16x32_f16 v[30:33], v[90:93], v[142:145], v[30:33]
	v_mfma_f32_16x16x32_f16 v[22:25], v[90:93], v[138:141], v[22:25]
	v_mfma_f32_16x16x32_f16 v[78:81], v[90:93], v[134:137], v[78:81]
	v_mfma_f32_16x16x32_f16 v[74:77], v[94:97], v[134:137], v[74:77]
	v_mfma_f32_16x16x32_f16 v[18:21], v[94:97], v[138:141], v[18:21]
	v_mfma_f32_16x16x32_f16 v[26:29], v[94:97], v[142:145], v[26:29]
	v_mfma_f32_16x16x32_f16 v[240:243], v[98:101], v[142:145], v[240:243]
	v_mfma_f32_16x16x32_f16 v[46:49], v[98:101], v[138:141], v[46:49]
	v_mfma_f32_16x16x32_f16 v[70:73], v[98:101], v[134:137], v[70:73]
	v_mfma_f32_16x16x32_f16 v[66:69], v[102:105], v[134:137], v[66:69]
	v_mfma_f32_16x16x32_f16 v[42:45], v[102:105], v[138:141], v[42:45]
	v_mfma_f32_16x16x32_f16 v[236:239], v[102:105], v[142:145], v[236:239]
	v_mfma_f32_16x16x32_f16 v[34:37], v[106:109], v[142:145], v[34:37]
	v_mfma_f32_16x16x32_f16 v[38:41], v[106:109], v[138:141], v[38:41]
	v_mfma_f32_16x16x32_f16 v[62:65], v[106:109], v[134:137], v[62:65]
	s_waitcnt lgkmcnt(0)
	v_mfma_f32_16x16x32_f16 v[82:85], v[110:113], v[146:149], v[82:85]
	v_mfma_f32_16x16x32_f16 v[58:61], v[110:113], v[150:153], v[58:61]
	v_mfma_f32_16x16x32_f16 v[14:17], v[110:113], v[154:157], v[14:17]
	v_mfma_f32_16x16x32_f16 v[30:33], v[114:117], v[154:157], v[30:33]
	v_mfma_f32_16x16x32_f16 v[22:25], v[114:117], v[150:153], v[22:25]
	v_mfma_f32_16x16x32_f16 v[78:81], v[114:117], v[146:149], v[78:81]
	v_mfma_f32_16x16x32_f16 v[74:77], v[118:121], v[146:149], v[74:77]
	v_mfma_f32_16x16x32_f16 v[18:21], v[118:121], v[150:153], v[18:21]
	v_mfma_f32_16x16x32_f16 v[26:29], v[118:121], v[154:157], v[26:29]
	v_mfma_f32_16x16x32_f16 v[240:243], v[122:125], v[154:157], v[240:243]
	v_mfma_f32_16x16x32_f16 v[46:49], v[122:125], v[150:153], v[46:49]
	v_mfma_f32_16x16x32_f16 v[70:73], v[122:125], v[146:149], v[70:73]
	v_mfma_f32_16x16x32_f16 v[66:69], v[126:129], v[146:149], v[66:69]
	v_mfma_f32_16x16x32_f16 v[42:45], v[126:129], v[150:153], v[42:45]
	v_mfma_f32_16x16x32_f16 v[236:239], v[126:129], v[154:157], v[236:239]
	v_mfma_f32_16x16x32_f16 v[34:37], v[130:133], v[154:157], v[34:37]
	v_mfma_f32_16x16x32_f16 v[38:41], v[130:133], v[150:153], v[38:41]
	v_mfma_f32_16x16x32_f16 v[62:65], v[130:133], v[146:149], v[62:65]
